# agg_ln1: selfp row load hoisted next to the cnt4/off4 loads (one dependent memory round trip fewer per node)
# speedup vs baseline: 1.1162x; 1.0074x over previous
_Z7agg_ln1PKDF16_S0_S0_PKiS2_S2_PKfS4_S4_PDF16_S4_S4_S5_S5_:
	s_cmpk_gt_u32 s2, 0xff
	s_mov_b64 s[4:5], -1
	s_cbranch_scc0 .LBB1_28
	v_lshl_or_b32 v1, s2, 8, v0
	v_add_u32_e32 v1, 0xffff0000, v1
	s_mov_b32 s3, 0x9c400
	v_cmp_gt_u32_e32 vcc, s3, v1
	s_and_saveexec_b64 s[18:19], vcc
	s_cbranch_execz .LBB1_27
	s_load_dwordx2 s[4:5], s[0:1], 0x20
	s_load_dwordx2 s[6:7], s[0:1], 0x18
	s_load_dwordx2 s[32:33], s[0:1], 0x8
	v_lshrrev_b32_e32 v1, 6, v1
	v_lshlrev_b32_e32 v2, 4, v1
	v_and_b32_e32 v24, 63, v0
	v_lshlrev_b32_e32 v8, 3, v24
	v_lshlrev_b32_e32 v21, 10, v1
	v_lshl_add_u32 v21, v24, 4, v21
	s_waitcnt lgkmcnt(0)
	global_load_dwordx4 v[28:31], v2, s[6:7]
	global_load_dwordx4 v[2:5], v2, s[4:5]
	global_load_dwordx4 v[60:63], v21, s[32:33] nt
	s_waitcnt vmcnt(0)
	v_add_u32_e32 v26, v3, v2
	v_add_u32_e32 v3, v26, v4
	v_add_u32_e32 v25, v3, v5
	v_cmp_gt_i32_e32 vcc, 1, v25
	s_and_saveexec_b64 s[4:5], vcc
	s_xor_b64 s[4:5], exec, s[4:5]
	v_mov_b32_e32 v9, 0
	s_or_saveexec_b64 s[22:23], s[4:5]
	s_load_dwordx2 s[20:21], s[0:1], 0x48
	v_mov_b32_e32 v11, 0
	v_mov_b64_e32 v[18:19], 0
	v_mov_b32_e32 v10, v11
	v_mov_b32_e32 v13, v11
	v_mov_b32_e32 v12, v11
	v_mov_b32_e32 v15, v11
	v_mov_b32_e32 v14, v11
	v_mov_b32_e32 v17, v11
	v_mov_b32_e32 v16, v11
	s_xor_b64 exec, exec, s[22:23]
	s_cbranch_execz .LBB1_26
	s_load_dwordx2 s[24:25], s[0:1], 0x28
	s_load_dwordx2 s[26:27], s[0:1], 0x0
	v_readfirstlane_b32 s2, v25
	v_readfirstlane_b32 s4, v2
	v_readfirstlane_b32 s5, v26
	v_readfirstlane_b32 s6, v3
	v_readfirstlane_b32 s8, v28
	v_readfirstlane_b32 s9, v29
	v_readfirstlane_b32 s10, v30
	v_readfirstlane_b32 s11, v31
	v_lshrrev_b32_e32 v20, 3, v24
	v_lshlrev_b32_e32 v20, 2, v20
	v_mov_b32_e32 v9, 0
	v_mov_b32_e32 v10, 0
	v_mov_b32_e32 v11, 0
	v_mov_b32_e32 v12, 0
	v_mov_b32_e32 v13, 0
	v_mov_b32_e32 v14, 0
	v_mov_b32_e32 v15, 0
	v_mov_b32_e32 v16, 0
	v_mov_b32_e32 v17, 0
	s_sub_u32 s9, s9, s4
	s_sub_u32 s10, s10, s5
	s_sub_u32 s11, s11, s6
	s_mov_b64 s[12:13], 0
	s_mov_b32 s3, 0
	s_sub_u32 s7, s2, 1
	s_waitcnt lgkmcnt(0)

.Lagg_ld7:
	s_add_u32 s17, s15, 7
	v_readlane_b32 s28, v6, s17
	s_mul_i32 s29, s28, 0x220
	s_add_u32 s54, s26, s29
	s_addc_u32 s55, s27, 0
	s_and_b32 s30, s28, 3
	s_lshl_b32 s30, s30, 4
	s_lshl_b64 s[30:31], 1, s30
	s_add_u32 s12, s12, s30
	s_addc_u32 s13, s13, s31
	global_load_dwordx2 v[54:55], v8, s[54:55]
	global_load_dword v39, v20, s[54:55] offset:512
.Lagg_ld6:
	s_add_u32 s17, s15, 6
	v_readlane_b32 s28, v6, s17
	s_mul_i32 s29, s28, 0x220
	s_add_u32 s52, s26, s29
	s_addc_u32 s53, s27, 0
	s_and_b32 s30, s28, 3
	s_lshl_b32 s30, s30, 4
	s_lshl_b64 s[30:31], 1, s30
	s_add_u32 s12, s12, s30
	s_addc_u32 s13, s13, s31
	global_load_dwordx2 v[52:53], v8, s[52:53]
	global_load_dword v38, v20, s[52:53] offset:512
.Lagg_ld5:
	s_add_u32 s17, s15, 5
	v_readlane_b32 s28, v6, s17
	s_mul_i32 s29, s28, 0x220
	s_add_u32 s50, s26, s29
	s_addc_u32 s51, s27, 0
	s_and_b32 s30, s28, 3
	s_lshl_b32 s30, s30, 4
	s_lshl_b64 s[30:31], 1, s30
	s_add_u32 s12, s12, s30
	s_addc_u32 s13, s13, s31
	global_load_dwordx2 v[50:51], v8, s[50:51]
	global_load_dword v37, v20, s[50:51] offset:512
.Lagg_ld4:
	s_add_u32 s17, s15, 4
	v_readlane_b32 s28, v6, s17
	s_mul_i32 s29, s28, 0x220
	s_add_u32 s48, s26, s29
	s_addc_u32 s49, s27, 0
	s_and_b32 s30, s28, 3
	s_lshl_b32 s30, s30, 4
	s_lshl_b64 s[30:31], 1, s30
	s_add_u32 s12, s12, s30
	s_addc_u32 s13, s13, s31
	global_load_dwordx2 v[48:49], v8, s[48:49]
	global_load_dword v36, v20, s[48:49] offset:512
.Lagg_ld3:
	s_add_u32 s17, s15, 3
	v_readlane_b32 s28, v6, s17
	s_mul_i32 s29, s28, 0x220
	s_add_u32 s46, s26, s29
	s_addc_u32 s47, s27, 0
	s_and_b32 s30, s28, 3
	s_lshl_b32 s30, s30, 4
	s_lshl_b64 s[30:31], 1, s30
	s_add_u32 s12, s12, s30
	s_addc_u32 s13, s13, s31
	global_load_dwordx2 v[46:47], v8, s[46:47]
	global_load_dword v35, v20, s[46:47] offset:512
.Lagg_ld2:
	s_add_u32 s17, s15, 2
	v_readlane_b32 s28, v6, s17
	s_mul_i32 s29, s28, 0x220
	s_add_u32 s44, s26, s29
	s_addc_u32 s45, s27, 0
	s_and_b32 s30, s28, 3
	s_lshl_b32 s30, s30, 4
	s_lshl_b64 s[30:31], 1, s30
	s_add_u32 s12, s12, s30
	s_addc_u32 s13, s13, s31
	global_load_dwordx2 v[44:45], v8, s[44:45]
	global_load_dword v34, v20, s[44:45] offset:512
.Lagg_ld1:
	s_add_u32 s17, s15, 1
	v_readlane_b32 s28, v6, s17
	s_mul_i32 s29, s28, 0x220
	s_add_u32 s42, s26, s29
	s_addc_u32 s43, s27, 0
	s_and_b32 s30, s28, 3
	s_lshl_b32 s30, s30, 4
	s_lshl_b64 s[30:31], 1, s30
	s_add_u32 s12, s12, s30
	s_addc_u32 s13, s13, s31
	global_load_dwordx2 v[42:43], v8, s[42:43]
	global_load_dword v33, v20, s[42:43] offset:512
.Lagg_ld0:
	s_add_u32 s17, s15, 0
	v_readlane_b32 s28, v6, s17
	s_mul_i32 s29, s28, 0x220
	s_add_u32 s40, s26, s29
	s_addc_u32 s41, s27, 0
	s_and_b32 s30, s28, 3
	s_lshl_b32 s30, s30, 4
	s_lshl_b64 s[30:31], 1, s30
	s_add_u32 s12, s12, s30
	s_addc_u32 s13, s13, s31
	global_load_dwordx2 v[40:41], v8, s[40:41]
	global_load_dword v32, v20, s[40:41] offset:512
	s_cmp_ge_u32 s16, 8
	s_cbranch_scc1 .Lagg_ac7
	s_cmp_ge_u32 s16, 7
	s_cbranch_scc1 .Lagg_ac6
	s_cmp_ge_u32 s16, 6
	s_cbranch_scc1 .Lagg_ac5
	s_cmp_ge_u32 s16, 5
	s_cbranch_scc1 .Lagg_ac4
	s_cmp_ge_u32 s16, 4
	s_cbranch_scc1 .Lagg_ac3
	s_cmp_ge_u32 s16, 3
	s_cbranch_scc1 .Lagg_ac2
	s_cmp_ge_u32 s16, 2
	s_cbranch_scc1 .Lagg_ac1
	s_branch .Lagg_ac0
.Lagg_ac7:
	s_waitcnt vmcnt(14)
	v_cvt_f32_i32_sdwa v2, sext(v54) dst_sel:DWORD dst_unused:UNUSED_PAD src0_sel:BYTE_0
	v_cvt_f32_i32_sdwa v3, sext(v54) dst_sel:DWORD dst_unused:UNUSED_PAD src0_sel:BYTE_1
	v_cvt_f32_i32_sdwa v22, sext(v54) dst_sel:DWORD dst_unused:UNUSED_PAD src0_sel:BYTE_2
	v_cvt_f32_i32_sdwa v23, sext(v54) dst_sel:DWORD dst_unused:UNUSED_PAD src0_sel:BYTE_3
	v_cvt_f32_i32_sdwa v26, sext(v55) dst_sel:DWORD dst_unused:UNUSED_PAD src0_sel:BYTE_0
	v_cvt_f32_i32_sdwa v27, sext(v55) dst_sel:DWORD dst_unused:UNUSED_PAD src0_sel:BYTE_1
	v_cvt_f32_i32_sdwa v28, sext(v55) dst_sel:DWORD dst_unused:UNUSED_PAD src0_sel:BYTE_2
	v_cvt_f32_i32_sdwa v29, sext(v55) dst_sel:DWORD dst_unused:UNUSED_PAD src0_sel:BYTE_3
	v_pk_fma_f32 v[16:17], v[38:39], v[2:3], v[16:17] op_sel:[1,0,0] op_sel_hi:[1,1,1]
	v_pk_fma_f32 v[14:15], v[38:39], v[22:23], v[14:15] op_sel:[1,0,0] op_sel_hi:[1,1,1]
	v_pk_fma_f32 v[12:13], v[38:39], v[26:27], v[12:13] op_sel:[1,0,0] op_sel_hi:[1,1,1]
	v_pk_fma_f32 v[10:11], v[38:39], v[28:29], v[10:11] op_sel:[1,0,0] op_sel_hi:[1,1,1]
.Lagg_ac6:
	s_waitcnt vmcnt(12)
	v_cvt_f32_i32_sdwa v2, sext(v52) dst_sel:DWORD dst_unused:UNUSED_PAD src0_sel:BYTE_0
	v_cvt_f32_i32_sdwa v3, sext(v52) dst_sel:DWORD dst_unused:UNUSED_PAD src0_sel:BYTE_1
	v_cvt_f32_i32_sdwa v22, sext(v52) dst_sel:DWORD dst_unused:UNUSED_PAD src0_sel:BYTE_2
	v_cvt_f32_i32_sdwa v23, sext(v52) dst_sel:DWORD dst_unused:UNUSED_PAD src0_sel:BYTE_3
	v_cvt_f32_i32_sdwa v26, sext(v53) dst_sel:DWORD dst_unused:UNUSED_PAD src0_sel:BYTE_0
	v_cvt_f32_i32_sdwa v27, sext(v53) dst_sel:DWORD dst_unused:UNUSED_PAD src0_sel:BYTE_1
	v_cvt_f32_i32_sdwa v28, sext(v53) dst_sel:DWORD dst_unused:UNUSED_PAD src0_sel:BYTE_2
	v_cvt_f32_i32_sdwa v29, sext(v53) dst_sel:DWORD dst_unused:UNUSED_PAD src0_sel:BYTE_3
	v_pk_fma_f32 v[16:17], v[38:39], v[2:3], v[16:17] op_sel_hi:[0,1,1]
	v_pk_fma_f32 v[14:15], v[38:39], v[22:23], v[14:15] op_sel_hi:[0,1,1]
	v_pk_fma_f32 v[12:13], v[38:39], v[26:27], v[12:13] op_sel_hi:[0,1,1]
	v_pk_fma_f32 v[10:11], v[38:39], v[28:29], v[10:11] op_sel_hi:[0,1,1]
.Lagg_ac5:
	s_waitcnt vmcnt(10)
	v_cvt_f32_i32_sdwa v2, sext(v50) dst_sel:DWORD dst_unused:UNUSED_PAD src0_sel:BYTE_0
	v_cvt_f32_i32_sdwa v3, sext(v50) dst_sel:DWORD dst_unused:UNUSED_PAD src0_sel:BYTE_1
	v_cvt_f32_i32_sdwa v22, sext(v50) dst_sel:DWORD dst_unused:UNUSED_PAD src0_sel:BYTE_2
	v_cvt_f32_i32_sdwa v23, sext(v50) dst_sel:DWORD dst_unused:UNUSED_PAD src0_sel:BYTE_3
	v_cvt_f32_i32_sdwa v26, sext(v51) dst_sel:DWORD dst_unused:UNUSED_PAD src0_sel:BYTE_0
	v_cvt_f32_i32_sdwa v27, sext(v51) dst_sel:DWORD dst_unused:UNUSED_PAD src0_sel:BYTE_1
	v_cvt_f32_i32_sdwa v28, sext(v51) dst_sel:DWORD dst_unused:UNUSED_PAD src0_sel:BYTE_2
	v_cvt_f32_i32_sdwa v29, sext(v51) dst_sel:DWORD dst_unused:UNUSED_PAD src0_sel:BYTE_3
	v_pk_fma_f32 v[16:17], v[36:37], v[2:3], v[16:17] op_sel:[1,0,0] op_sel_hi:[1,1,1]
	v_pk_fma_f32 v[14:15], v[36:37], v[22:23], v[14:15] op_sel:[1,0,0] op_sel_hi:[1,1,1]
	v_pk_fma_f32 v[12:13], v[36:37], v[26:27], v[12:13] op_sel:[1,0,0] op_sel_hi:[1,1,1]
	v_pk_fma_f32 v[10:11], v[36:37], v[28:29], v[10:11] op_sel:[1,0,0] op_sel_hi:[1,1,1]
.Lagg_ac4:
	s_waitcnt vmcnt(8)
	v_cvt_f32_i32_sdwa v2, sext(v48) dst_sel:DWORD dst_unused:UNUSED_PAD src0_sel:BYTE_0
	v_cvt_f32_i32_sdwa v3, sext(v48) dst_sel:DWORD dst_unused:UNUSED_PAD src0_sel:BYTE_1
	v_cvt_f32_i32_sdwa v22, sext(v48) dst_sel:DWORD dst_unused:UNUSED_PAD src0_sel:BYTE_2
	v_cvt_f32_i32_sdwa v23, sext(v48) dst_sel:DWORD dst_unused:UNUSED_PAD src0_sel:BYTE_3
	v_cvt_f32_i32_sdwa v26, sext(v49) dst_sel:DWORD dst_unused:UNUSED_PAD src0_sel:BYTE_0
	v_cvt_f32_i32_sdwa v27, sext(v49) dst_sel:DWORD dst_unused:UNUSED_PAD src0_sel:BYTE_1
	v_cvt_f32_i32_sdwa v28, sext(v49) dst_sel:DWORD dst_unused:UNUSED_PAD src0_sel:BYTE_2
	v_cvt_f32_i32_sdwa v29, sext(v49) dst_sel:DWORD dst_unused:UNUSED_PAD src0_sel:BYTE_3
	v_pk_fma_f32 v[16:17], v[36:37], v[2:3], v[16:17] op_sel_hi:[0,1,1]
	v_pk_fma_f32 v[14:15], v[36:37], v[22:23], v[14:15] op_sel_hi:[0,1,1]
	v_pk_fma_f32 v[12:13], v[36:37], v[26:27], v[12:13] op_sel_hi:[0,1,1]
	v_pk_fma_f32 v[10:11], v[36:37], v[28:29], v[10:11] op_sel_hi:[0,1,1]
.Lagg_ac3:
	s_waitcnt vmcnt(6)
	v_cvt_f32_i32_sdwa v2, sext(v46) dst_sel:DWORD dst_unused:UNUSED_PAD src0_sel:BYTE_0
	v_cvt_f32_i32_sdwa v3, sext(v46) dst_sel:DWORD dst_unused:UNUSED_PAD src0_sel:BYTE_1
	v_cvt_f32_i32_sdwa v22, sext(v46) dst_sel:DWORD dst_unused:UNUSED_PAD src0_sel:BYTE_2
	v_cvt_f32_i32_sdwa v23, sext(v46) dst_sel:DWORD dst_unused:UNUSED_PAD src0_sel:BYTE_3
	v_cvt_f32_i32_sdwa v26, sext(v47) dst_sel:DWORD dst_unused:UNUSED_PAD src0_sel:BYTE_0
	v_cvt_f32_i32_sdwa v27, sext(v47) dst_sel:DWORD dst_unused:UNUSED_PAD src0_sel:BYTE_1
	v_cvt_f32_i32_sdwa v28, sext(v47) dst_sel:DWORD dst_unused:UNUSED_PAD src0_sel:BYTE_2
	v_cvt_f32_i32_sdwa v29, sext(v47) dst_sel:DWORD dst_unused:UNUSED_PAD src0_sel:BYTE_3
	v_pk_fma_f32 v[16:17], v[34:35], v[2:3], v[16:17] op_sel:[1,0,0] op_sel_hi:[1,1,1]
	v_pk_fma_f32 v[14:15], v[34:35], v[22:23], v[14:15] op_sel:[1,0,0] op_sel_hi:[1,1,1]
	v_pk_fma_f32 v[12:13], v[34:35], v[26:27], v[12:13] op_sel:[1,0,0] op_sel_hi:[1,1,1]
	v_pk_fma_f32 v[10:11], v[34:35], v[28:29], v[10:11] op_sel:[1,0,0] op_sel_hi:[1,1,1]
.Lagg_ac2:
	s_waitcnt vmcnt(4)
	v_cvt_f32_i32_sdwa v2, sext(v44) dst_sel:DWORD dst_unused:UNUSED_PAD src0_sel:BYTE_0
	v_cvt_f32_i32_sdwa v3, sext(v44) dst_sel:DWORD dst_unused:UNUSED_PAD src0_sel:BYTE_1
	v_cvt_f32_i32_sdwa v22, sext(v44) dst_sel:DWORD dst_unused:UNUSED_PAD src0_sel:BYTE_2
	v_cvt_f32_i32_sdwa v23, sext(v44) dst_sel:DWORD dst_unused:UNUSED_PAD src0_sel:BYTE_3
	v_cvt_f32_i32_sdwa v26, sext(v45) dst_sel:DWORD dst_unused:UNUSED_PAD src0_sel:BYTE_0
	v_cvt_f32_i32_sdwa v27, sext(v45) dst_sel:DWORD dst_unused:UNUSED_PAD src0_sel:BYTE_1
	v_cvt_f32_i32_sdwa v28, sext(v45) dst_sel:DWORD dst_unused:UNUSED_PAD src0_sel:BYTE_2
	v_cvt_f32_i32_sdwa v29, sext(v45) dst_sel:DWORD dst_unused:UNUSED_PAD src0_sel:BYTE_3
	v_pk_fma_f32 v[16:17], v[34:35], v[2:3], v[16:17] op_sel_hi:[0,1,1]
	v_pk_fma_f32 v[14:15], v[34:35], v[22:23], v[14:15] op_sel_hi:[0,1,1]
	v_pk_fma_f32 v[12:13], v[34:35], v[26:27], v[12:13] op_sel_hi:[0,1,1]
	v_pk_fma_f32 v[10:11], v[34:35], v[28:29], v[10:11] op_sel_hi:[0,1,1]
.Lagg_ac1:
	s_waitcnt vmcnt(2)
	v_cvt_f32_i32_sdwa v2, sext(v42) dst_sel:DWORD dst_unused:UNUSED_PAD src0_sel:BYTE_0
	v_cvt_f32_i32_sdwa v3, sext(v42) dst_sel:DWORD dst_unused:UNUSED_PAD src0_sel:BYTE_1
	v_cvt_f32_i32_sdwa v22, sext(v42) dst_sel:DWORD dst_unused:UNUSED_PAD src0_sel:BYTE_2
	v_cvt_f32_i32_sdwa v23, sext(v42) dst_sel:DWORD dst_unused:UNUSED_PAD src0_sel:BYTE_3
	v_cvt_f32_i32_sdwa v26, sext(v43) dst_sel:DWORD dst_unused:UNUSED_PAD src0_sel:BYTE_0
	v_cvt_f32_i32_sdwa v27, sext(v43) dst_sel:DWORD dst_unused:UNUSED_PAD src0_sel:BYTE_1
	v_cvt_f32_i32_sdwa v28, sext(v43) dst_sel:DWORD dst_unused:UNUSED_PAD src0_sel:BYTE_2
	v_cvt_f32_i32_sdwa v29, sext(v43) dst_sel:DWORD dst_unused:UNUSED_PAD src0_sel:BYTE_3
	v_pk_fma_f32 v[16:17], v[32:33], v[2:3], v[16:17] op_sel:[1,0,0] op_sel_hi:[1,1,1]
	v_pk_fma_f32 v[14:15], v[32:33], v[22:23], v[14:15] op_sel:[1,0,0] op_sel_hi:[1,1,1]
	v_pk_fma_f32 v[12:13], v[32:33], v[26:27], v[12:13] op_sel:[1,0,0] op_sel_hi:[1,1,1]
	v_pk_fma_f32 v[10:11], v[32:33], v[28:29], v[10:11] op_sel:[1,0,0] op_sel_hi:[1,1,1]
.Lagg_ac0:
	s_waitcnt vmcnt(0)
	v_cvt_f32_i32_sdwa v2, sext(v40) dst_sel:DWORD dst_unused:UNUSED_PAD src0_sel:BYTE_0
	v_cvt_f32_i32_sdwa v3, sext(v40) dst_sel:DWORD dst_unused:UNUSED_PAD src0_sel:BYTE_1
	v_cvt_f32_i32_sdwa v22, sext(v40) dst_sel:DWORD dst_unused:UNUSED_PAD src0_sel:BYTE_2
	v_cvt_f32_i32_sdwa v23, sext(v40) dst_sel:DWORD dst_unused:UNUSED_PAD src0_sel:BYTE_3
	v_cvt_f32_i32_sdwa v26, sext(v41) dst_sel:DWORD dst_unused:UNUSED_PAD src0_sel:BYTE_0
	v_cvt_f32_i32_sdwa v27, sext(v41) dst_sel:DWORD dst_unused:UNUSED_PAD src0_sel:BYTE_1
	v_cvt_f32_i32_sdwa v28, sext(v41) dst_sel:DWORD dst_unused:UNUSED_PAD src0_sel:BYTE_2
	v_cvt_f32_i32_sdwa v29, sext(v41) dst_sel:DWORD dst_unused:UNUSED_PAD src0_sel:BYTE_3
	v_pk_fma_f32 v[16:17], v[32:33], v[2:3], v[16:17] op_sel_hi:[0,1,1]
	v_pk_fma_f32 v[14:15], v[32:33], v[22:23], v[14:15] op_sel_hi:[0,1,1]
	v_pk_fma_f32 v[12:13], v[32:33], v[26:27], v[12:13] op_sel_hi:[0,1,1]
	v_pk_fma_f32 v[10:11], v[32:33], v[28:29], v[10:11] op_sel_hi:[0,1,1]
	s_add_u32 s15, s15, 8
	s_cmp_lt_u32 s15, s14
	s_cbranch_scc1 .Lagg_inner
	s_add_u32 s3, s3, 64
	s_cmp_lt_u32 s3, s2
	s_cbranch_scc1 .Lagg_outer
	v_mov_b32_e32 v18, s12
	v_mov_b32_e32 v19, s13
.LBB1_26:
	s_or_b64 exec, exec, s[22:23]
	s_load_dwordx2 s[8:9], s[0:1], 0x40
	s_load_dwordx2 s[10:11], s[0:1], 0x8
	s_load_dwordx4 s[4:7], s[0:1], 0x30
	v_lshlrev_b64 v[44:45], 2, v[8:9]
	v_lshlrev_b32_e32 v42, 10, v1
	v_mov_b32_e32 v43, 0
	s_waitcnt lgkmcnt(0)
	v_lshl_add_u64 v[6:7], s[10:11], 0, v[42:43]
	v_lshl_add_u64 v[34:35], s[4:5], 0, v[44:45]
	global_load_dwordx4 v[2:5], v[34:35], off offset:2048
	v_lshl_add_u64 v[36:37], v[8:9], 1, v[6:7]
	global_load_dwordx4 v[20:23], v[34:35], off
	global_load_dwordx4 v[26:29], v[34:35], off offset:16
	global_load_dwordx4 v[30:33], v[34:35], off offset:2064
	s_movk_i32 s12, 0x1000
	v_add_co_u32_e32 v52, vcc, s12, v34
	s_mov_b64 s[4:5], 0x1000
	s_mov_b64 s[10:11], 0x1800
	v_addc_co_u32_e32 v53, vcc, 0, v35, vcc
	v_lshl_add_u64 v[48:49], v[34:35], 0, s[4:5]
	v_lshl_add_u64 v[50:51], v[34:35], 0, s[10:11]
	global_load_dwordx4 v[34:37], v[52:53], off
	global_load_dwordx4 v[38:41], v[52:53], off offset:2048
	v_max_i32_e32 v25, 1, v25
	v_cvt_f32_u32_e32 v25, v25
	s_flbit_i32_b32 s3, 0
	v_lshrrev_b32_e32 v42, 16, v19
	s_min_u32 s3, s3, 32
	v_lshlrev_b64 v[46:47], s3, v[42:43]
	v_min_u32_e32 v42, 1, v46
	v_div_scale_f32 v46, s[4:5], v25, v25, 1.0
	v_rcp_f32_e32 v52, v46
	v_or_b32_e32 v47, v47, v42
	v_div_scale_f32 v42, vcc, 1.0, v25, 1.0
	v_fma_f32 v53, -v46, v52, 1.0
	v_fmac_f32_e32 v52, v53, v52
	v_mul_f32_e32 v53, v42, v52
	v_fma_f32 v55, -v46, v53, v42
	v_cvt_f32_u32_sdwa v54, v18 dst_sel:DWORD dst_unused:UNUSED_PAD src0_sel:WORD_0
	v_cvt_f32_u32_sdwa v18, v18 dst_sel:DWORD dst_unused:UNUSED_PAD src0_sel:WORD_1
	v_fmac_f32_e32 v53, v55, v52
	v_fma_f32 v42, -v46, v53, v42
	v_div_fmas_f32 v42, v42, v52, v53
	v_div_fixup_f32 v42, v42, v25, 1.0
	v_mul_f32_e32 v52, v42, v18
	v_mul_f32_e32 v46, v42, v54
	v_cvt_f32_u32_sdwa v18, v19 dst_sel:DWORD dst_unused:UNUSED_PAD src0_sel:WORD_0
	v_cvt_f32_u32_e32 v25, v47
	s_sub_i32 s3, 32, s3
	v_ldexp_f32 v25, v25, s3
	s_waitcnt vmcnt(5)
	v_cvt_f32_f16_e32 v54, v60
	v_pk_mul_f32 v[2:3], v[52:53], v[2:3] op_sel_hi:[0,1]
	v_pk_mul_f32 v[4:5], v[52:53], v[4:5] op_sel_hi:[0,1]
	v_cvt_f32_f16_sdwa v55, v60 dst_sel:DWORD dst_unused:UNUSED_PAD src0_sel:WORD_1
	s_waitcnt vmcnt(4)
	v_pk_fma_f32 v[20:21], v[46:47], v[20:21], v[2:3] op_sel_hi:[0,1,1]
	v_cvt_f32_f16_e32 v56, v61
	v_cvt_f32_f16_sdwa v57, v61 dst_sel:DWORD dst_unused:UNUSED_PAD src0_sel:WORD_1
	v_pk_fma_f32 v[22:23], v[46:47], v[22:23], v[4:5] op_sel_hi:[0,1,1]
	v_cvt_f32_f16_e32 v58, v62
	v_cvt_f32_f16_sdwa v59, v62 dst_sel:DWORD dst_unused:UNUSED_PAD src0_sel:WORD_1
	v_cvt_f32_f16_e32 v60, v63
	v_cvt_f32_f16_sdwa v61, v63 dst_sel:DWORD dst_unused:UNUSED_PAD src0_sel:WORD_1
	global_load_dwordx4 v[2:5], v[48:49], off offset:16
	global_load_dwordx4 v[6:9], v[50:51], off offset:16
	v_mul_f32_e32 v48, v42, v18
	s_waitcnt vmcnt(3)
	v_pk_fma_f32 v[18:19], v[48:49], v[34:35], v[20:21] op_sel_hi:[0,1,1]
	v_pk_fma_f32 v[20:21], v[48:49], v[36:37], v[22:23] op_sel_hi:[0,1,1]
	v_mul_f32_e32 v50, v42, v25
	v_lshl_add_u64 v[22:23], s[6:7], 0, v[44:45]
	v_lshl_add_u64 v[44:45], s[8:9], 0, v[44:45]
	s_waitcnt vmcnt(2)
	v_pk_fma_f32 v[38:39], v[50:51], v[38:39], v[18:19] op_sel_hi:[0,1,1]
	v_pk_fma_f32 v[62:63], v[50:51], v[40:41], v[20:21] op_sel_hi:[0,1,1]
	v_pk_fma_f32 v[40:41], v[16:17], v[42:43], v[54:55] op_sel_hi:[1,0,1]
	global_load_dwordx4 v[18:21], v[22:23], off
	global_load_dwordx4 v[34:37], v[22:23], off offset:16
	v_pk_fma_f32 v[54:55], v[14:15], v[42:43], v[56:57] op_sel_hi:[1,0,1]
	global_load_dwordx4 v[14:17], v[44:45], off
	v_pk_add_f32 v[22:23], v[40:41], v[38:39]
	global_load_dwordx4 v[38:41], v[44:45], off offset:16
	v_pk_mul_f32 v[30:31], v[52:53], v[30:31] op_sel_hi:[0,1]
	v_pk_fma_f32 v[26:27], v[46:47], v[26:27], v[30:31] op_sel_hi:[0,1,1]
	v_pk_add_f32 v[44:45], v[62:63], v[54:55]
	v_pk_fma_f32 v[12:13], v[12:13], v[42:43], v[58:59] op_sel_hi:[1,0,1]
	v_mov_b32_e32 v25, 0x3b000000
	s_waitcnt vmcnt(5)
	v_pk_fma_f32 v[2:3], v[48:49], v[2:3], v[26:27] op_sel_hi:[0,1,1]
	s_waitcnt vmcnt(4)
	v_pk_fma_f32 v[2:3], v[50:51], v[6:7], v[2:3] op_sel_hi:[0,1,1]
	v_add_f32_e32 v6, 0, v22
	v_add_f32_e32 v6, v6, v23
	v_add_f32_e32 v6, v6, v44
	v_add_f32_e32 v6, v6, v45
	v_pk_add_f32 v[2:3], v[12:13], v[2:3]
	s_nop 0
	v_add_f32_e32 v6, v6, v2
	v_add_f32_e32 v12, v6, v3
	v_pk_fma_f32 v[6:7], v[10:11], v[42:43], v[60:61] op_sel_hi:[1,0,1]
	v_pk_mul_f32 v[10:11], v[52:53], v[32:33] op_sel_hi:[0,1]
	v_pk_fma_f32 v[10:11], v[46:47], v[28:29], v[10:11] op_sel_hi:[0,1,1]
	v_pk_fma_f32 v[4:5], v[48:49], v[4:5], v[10:11] op_sel_hi:[0,1,1]
	v_pk_fma_f32 v[4:5], v[50:51], v[8:9], v[4:5] op_sel_hi:[0,1,1]
	v_pk_add_f32 v[4:5], v[4:5], v[6:7]
	v_mov_b32_e32 v7, v43
	v_add_f32_e32 v6, v12, v4
	v_add_f32_e32 v6, v6, v5
	s_nop 1
	v_add_f32_dpp v6, v6, v6 quad_perm:[1,0,3,2] row_mask:0xf bank_mask:0xf bound_ctrl:1
	s_nop 1
	v_add_f32_dpp v6, v6, v6 quad_perm:[2,3,0,1] row_mask:0xf bank_mask:0xf bound_ctrl:1
	s_nop 1
	v_add_f32_dpp v6, v6, v6 row_half_mirror row_mask:0xf bank_mask:0xf bound_ctrl:1
	s_nop 1
	v_add_f32_dpp v6, v6, v6 row_mirror row_mask:0xf bank_mask:0xf bound_ctrl:1
	s_nop 1
	v_mov_b32_dpp v7, v6 row_bcast:15 row_mask:0xa bank_mask:0xf
	v_add_f32_e32 v6, v6, v7
	v_mov_b32_e32 v7, v43
	s_nop 1
	v_mov_b32_dpp v7, v6 row_bcast:31 row_mask:0xc bank_mask:0xf
	v_add_f32_e32 v6, v6, v7
	s_nop 0
	v_readlane_b32 s3, v6, 63
	s_nop 1
	v_mul_f32_e32 v6, s3, v25
	v_pk_add_f32 v[8:9], v[22:23], v[6:7] op_sel_hi:[1,0] neg_lo:[0,1] neg_hi:[0,1]
	v_pk_add_f32 v[12:13], v[44:45], v[6:7] op_sel_hi:[1,0] neg_lo:[0,1] neg_hi:[0,1]
	v_pk_mul_f32 v[10:11], v[8:9], v[8:9]
	v_pk_mul_f32 v[22:23], v[12:13], v[12:13]
	v_add_f32_e32 v10, v10, v11
	v_pk_add_f32 v[2:3], v[2:3], v[6:7] op_sel_hi:[1,0] neg_lo:[0,1] neg_hi:[0,1]
	v_add_f32_e32 v10, v10, v22
	v_pk_mul_f32 v[26:27], v[2:3], v[2:3]
	v_add_f32_e32 v10, v10, v23
	v_pk_add_f32 v[4:5], v[4:5], v[6:7] op_sel_hi:[1,0] neg_lo:[0,1] neg_hi:[0,1]
	v_add_f32_e32 v10, v10, v26
	v_pk_mul_f32 v[6:7], v[4:5], v[4:5]
	v_add_f32_e32 v10, v10, v27
	v_add_f32_e32 v6, v10, v6
	v_add_f32_e32 v6, v6, v7
	v_mov_b32_e32 v7, v43
	s_nop 0
	v_add_f32_dpp v6, v6, v6 quad_perm:[1,0,3,2] row_mask:0xf bank_mask:0xf bound_ctrl:1
	s_nop 1
	v_add_f32_dpp v6, v6, v6 quad_perm:[2,3,0,1] row_mask:0xf bank_mask:0xf bound_ctrl:1
	s_nop 1
	v_add_f32_dpp v6, v6, v6 row_half_mirror row_mask:0xf bank_mask:0xf bound_ctrl:1
	s_nop 1
	v_add_f32_dpp v6, v6, v6 row_mirror row_mask:0xf bank_mask:0xf bound_ctrl:1
	s_nop 1
	v_mov_b32_dpp v7, v6 row_bcast:15 row_mask:0xa bank_mask:0xf
	v_add_f32_e32 v6, v6, v7
	s_nop 1
	v_mov_b32_dpp v43, v6 row_bcast:31 row_mask:0xc bank_mask:0xf
	v_add_f32_e32 v6, v6, v43
	s_nop 0
	v_readlane_b32 s3, v6, 63
	v_mov_b32_e32 v6, 0x3727c5ac
	s_nop 0
	v_fmac_f32_e32 v6, s3, v25
	s_mov_b32 s3, 0x800000
	v_mul_f32_e32 v7, 0x4b800000, v6
	v_cmp_gt_f32_e32 vcc, s3, v6
	s_movk_i32 s3, 0x2800
	s_nop 0
	v_cndmask_b32_e32 v6, v6, v7, vcc
	v_rsq_f32_e32 v6, v6
	v_lshrrev_b32_e32 v7, 3, v24
	v_mad_u32_u24 v1, v7, s3, v1
	v_mul_f32_e32 v7, 0x45800000, v6
	v_cndmask_b32_e32 v6, v6, v7, vcc
	v_pk_mul_f32 v[2:3], v[2:3], v[6:7] op_sel_hi:[1,0]
	v_pk_mul_f32 v[10:11], v[12:13], v[6:7] op_sel_hi:[1,0]
	s_waitcnt vmcnt(0)
	v_pk_fma_f32 v[12:13], v[34:35], v[2:3], v[38:39]
	v_pk_mul_f32 v[2:3], v[4:5], v[6:7] op_sel_hi:[1,0]
	v_pk_mul_f32 v[8:9], v[8:9], v[6:7] op_sel_hi:[1,0]
	v_pk_fma_f32 v[6:7], v[36:37], v[2:3], v[40:41]
	v_pk_fma_f32 v[8:9], v[18:19], v[8:9], v[14:15]
	v_cvt_pk_f16_f32 v5, v6, v7
	v_lshlrev_b32_e32 v6, 4, v0
	v_pk_fma_f32 v[10:11], v[20:21], v[10:11], v[16:17]
	v_and_b32_e32 v6, 0x70, v6
	v_cvt_pk_f16_f32 v2, v8, v9
	v_cvt_pk_f16_f32 v3, v10, v11
	v_cvt_pk_f16_f32 v4, v12, v13
	v_lshl_or_b32 v1, v1, 7, v6
	global_store_dwordx4 v1, v[2:5], s[20:21]
